# rotary-key copy in phase L2: 12 loads prefetched together instead of 8 serialized round trips (with store-data WAR padding)
# speedup vs baseline: 1.0275x; 1.0044x over previous
; DEVI int opaque_tid() { int t = threadIdx.x; asm volatile("" : "+v"(t)); return t; }
; DEVI void phase_l2(const Params& p, int l, char* smem) {
;     ...
;     for (int i = 0; i < 4; ++i) {
;         pg8::Unit uk; if (!Skv.next(i, uk)) break;
;         const int pm = uk.pm, pn = uk.pn;
;         bf16_t* Kb = (bf16_t*)(p.ws + WS_K);
;         const int tid = opaque_tid(), rl = tid >> 1, half = tid & 1, row = pm * 256 + rl;
;         const bool lat = row < NLAT; const int b = lat ? (row >> 11) : ((row - NLAT) >> 8); const int t = lat ? (row & 2047) : ((row - NLAT) & 255);
;         const int kpos = lat ? (CL + t) : t;
;         bf16_t* dst = Kb + ((size_t)(b * 8 + pn) * KEYS + kpos) * 192 + 128 + half * 32;
; #pragma unroll
;         for (int q = 0; q < 4; ++q) {
;             float f[8]; unpack8(*(const bf16x8*)(P + (size_t)row * INC + C_KR + half * 32 + q * 8), f);
;             if (lat) {
; #pragma unroll
;                 for (int e = 0; e < 4; ++e) { const int pi = half * 16 + q * 4 + e; const int pos = (pi < 16) ? (t >> 6) : (t & 63);
;                     const f32x2 cs = *(const f32x2*)(rax + (pos * 16 + (pi & 15)) * 2);
;                     const float x1 = f[2 * e], x2 = f[2 * e + 1]; f[2 * e] = x1 * cs[0] - x2 * cs[1]; f[2 * e + 1] = x1 * cs[1] + x2 * cs[0]; }
;             }
;             *(bf16x8*)(dst + q * 8) = pack8(f);
;         }
;     }
.LBB0_481:
	v_mov_b32_e32 v1, v0
	s_waitcnt vmcnt(0)
	v_mov_b64_e32 v[4:5], s[86:87]
	v_ashrrev_i32_e32 v6, 1, v1
	v_and_b32_e32 v1, 1, v1
	v_lshl_add_u32 v9, s7, 8, v6
	v_mad_i64_i32 v[4:5], s[14:15], v9, s93, v[4:5]
	v_lshlrev_b32_e32 v2, 6, v1
	v_lshl_add_u64 v[4:5], v[4:5], 0, v[2:3]
	global_load_dwordx4 v[20:23], v[4:5], off offset:1536
	global_load_dwordx4 v[52:55], v[4:5], off offset:1552
	global_load_dwordx4 v[56:59], v[4:5], off offset:1568
	global_load_dwordx4 v[60:63], v[4:5], off offset:1584
	v_and_b32_e32 v2, 0xff, v6
	v_and_b32_e32 v15, 0x7ff, v9
	v_cmp_gt_i32_e32 vcc, s90, v9
	s_nop 1
	v_cndmask_b32_e32 v177, v2, v15, vcc
	v_cmp_eq_u32_e64 s[38:39], 0, v1
	v_lshrrev_b32_e32 v178, 6, v177
	v_and_b32_e32 v179, 63, v177
	v_cndmask_b32_e64 v176, v179, v178, s[38:39]
	v_lshlrev_b32_e32 v176, 7, v176
	global_load_dwordx4 v[64:67], v176, s[10:11] offset:16
	global_load_dwordx4 v[68:71], v176, s[10:11]
	global_load_dwordx4 v[72:75], v176, s[10:11] offset:48
	global_load_dwordx4 v[156:159], v176, s[10:11] offset:32
	global_load_dwordx4 v[160:163], v176, s[10:11] offset:80
	global_load_dwordx4 v[164:167], v176, s[10:11] offset:64
	global_load_dwordx4 v[168:171], v176, s[10:11] offset:112
	global_load_dwordx4 v[172:175], v176, s[10:11] offset:96
	s_waitcnt vmcnt(0)
	v_lshlrev_b32_e32 v7, 16, v23
	v_cndmask_b32_e32 v6, v2, v15, vcc
	v_lshrrev_b32_e32 v11, 6, v6
	v_and_b32_e32 v13, 63, v6
	v_and_b32_e32 v6, 0xffff0000, v23
	v_lshlrev_b32_e32 v12, 16, v20
	v_and_b32_e32 v20, 0xffff0000, v20
	v_lshlrev_b32_e32 v14, 16, v21
	v_and_b32_e32 v18, 0xffff0000, v21
	v_lshlrev_b32_e32 v8, 16, v22
	v_and_b32_e32 v10, 0xffff0000, v22
	v_pk_mov_b32 v[16:17], v[6:7], v[6:7] op_sel:[1,0]
	s_and_saveexec_b64 s[16:17], vcc
	s_cbranch_execz .LBB0_483
	v_cmp_eq_u32_e64 s[38:39], 0, v1
	s_nop 1
	v_cndmask_b32_e64 v16, v13, v11, s[38:39]
	v_lshlrev_b32_e32 v16, 7, v16
	s_nop 1
	v_mov_b64_e32 v[22:23], v[64:65]
	v_mov_b64_e32 v[24:25], v[66:67]
	s_nop 1
	v_mov_b64_e32 v[26:27], v[68:69]
	v_mov_b64_e32 v[28:29], v[70:71]
	v_pk_mul_f32 v[16:17], v[28:29], v[18:19] op_sel:[1,0] op_sel_hi:[0,0]
	v_pk_fma_f32 v[18:19], v[28:29], v[14:15], v[16:17] op_sel_hi:[1,0,1] neg_lo:[0,0,1] neg_hi:[0,0,1]
	v_pk_fma_f32 v[28:29], v[28:29], v[14:15], v[16:17] op_sel_hi:[1,0,1]
	v_pk_mul_f32 v[16:17], v[22:23], v[10:11] op_sel:[1,0] op_sel_hi:[0,0]
	v_pk_fma_f32 v[32:33], v[22:23], v[8:9], v[16:17] op_sel_hi:[1,0,1] neg_lo:[0,0,1] neg_hi:[0,0,1]
	v_pk_fma_f32 v[22:23], v[22:23], v[8:9], v[16:17] op_sel_hi:[1,0,1]
	v_mul_f32_e32 v8, v25, v6
	v_pk_mul_f32 v[20:21], v[26:27], v[20:21] op_sel:[1,0] op_sel_hi:[0,0]
	v_pk_fma_f32 v[16:17], v[24:25], v[6:7], v[8:9] op_sel:[0,1,0] op_sel_hi:[1,0,0] neg_lo:[0,0,1] neg_hi:[0,0,1]
	v_mul_f32_e32 v8, v25, v7
	v_pk_mul_f32 v[30:31], v[26:27], v[12:13] op_sel_hi:[1,0]
	v_pk_fma_f32 v[26:27], v[26:27], v[12:13], v[20:21] op_sel_hi:[1,0,1]
	v_pk_fma_f32 v[6:7], v[24:25], v[6:7], v[8:9] op_sel_hi:[1,1,0]
	v_sub_f32_e32 v12, v30, v20
	v_mov_b32_e32 v20, v27
	v_mov_b32_e32 v14, v18
	v_mov_b32_e32 v18, v29
	v_mov_b32_e32 v8, v32
	v_mov_b32_e32 v10, v23
	v_mov_b32_e32 v17, v6
.LBB0_483:
	s_or_b64 exec, exec, s[16:17]
	v_add_u32_e32 v7, 0xffffe000, v9
	v_ashrrev_i32_e32 v6, 11, v9
	v_lshrrev_b32_e32 v7, 8, v7
	v_cndmask_b32_e32 v6, v7, v6, vcc
	v_add_u32_e32 v7, 0x100, v15
	v_cndmask_b32_e32 v2, v2, v7, vcc
	v_lshl_add_u32 v6, v6, 3, s6
	v_mad_i64_i32 v[6:7], s[14:15], v6, s84, v[2:3]
	v_mov_b64_e32 v[22:23], s[82:83]
	v_lshlrev_b32_e32 v19, 5, v1
	v_mad_u64_u32 v[22:23], s[14:15], v6, s85, v[22:23]
	v_mad_i32_i24 v23, v7, s85, v23
	v_lshlrev_b32_e32 v2, 1, v19
	v_lshl_add_u64 v[6:7], v[22:23], 0, v[2:3]
	v_cvt_pk_bf16_f32 v21, v14, v18
	v_cvt_pk_bf16_f32 v23, v16, v17
	s_nop 1
	v_mov_b64_e32 v[14:15], v[52:53]
	v_mov_b64_e32 v[16:17], v[54:55]
	s_mov_b32 s14, 0x40fae000
	v_cvt_pk_bf16_f32 v22, v8, v10
	v_add_co_u32_e64 v8, s[38:39], s14, v6
	v_cvt_pk_bf16_f32 v20, v12, v20
	s_nop 0
	v_addc_co_u32_e64 v9, s[38:39], 0, v7, s[38:39]
	global_store_dwordx4 v[8:9], v[20:23], off offset:256
	v_lshlrev_b32_e32 v9, 16, v17
	v_and_b32_e32 v8, 0xffff0000, v17
	v_lshlrev_b32_e32 v12, 16, v14
	v_and_b32_e32 v20, 0xffff0000, v14
	v_lshlrev_b32_e32 v14, 16, v15
	v_and_b32_e32 v18, 0xffff0000, v15
	v_lshlrev_b32_e32 v2, 16, v16
	v_and_b32_e32 v10, 0xffff0000, v16
	v_pk_mov_b32 v[16:17], v[8:9], v[8:9] op_sel:[1,0]
	s_and_saveexec_b64 s[16:17], vcc
	s_cbranch_execz .LBB0_485
	v_cmp_eq_u32_e64 s[38:39], 0, v1
	s_nop 1
	v_cndmask_b32_e64 v15, v13, v11, s[38:39]
	v_lshlrev_b32_e32 v15, 7, v15
	s_nop 1
	v_mov_b64_e32 v[22:23], v[72:73]
	v_mov_b64_e32 v[24:25], v[74:75]
	s_nop 1
	v_mov_b64_e32 v[26:27], v[156:157]
	v_mov_b64_e32 v[28:29], v[158:159]
	v_pk_mul_f32 v[16:17], v[28:29], v[18:19] op_sel:[1,0] op_sel_hi:[0,0]
	v_pk_fma_f32 v[18:19], v[28:29], v[14:15], v[16:17] op_sel_hi:[1,0,1] neg_lo:[0,0,1] neg_hi:[0,0,1]
	v_pk_fma_f32 v[14:15], v[28:29], v[14:15], v[16:17] op_sel_hi:[1,0,1]
	v_pk_mul_f32 v[16:17], v[22:23], v[10:11] op_sel:[1,0] op_sel_hi:[0,0]
	v_pk_fma_f32 v[28:29], v[22:23], v[2:3], v[16:17] op_sel_hi:[1,0,1] neg_lo:[0,0,1] neg_hi:[0,0,1]
	v_pk_fma_f32 v[22:23], v[22:23], v[2:3], v[16:17] op_sel_hi:[1,0,1]
	v_mul_f32_e32 v2, v25, v8
	v_pk_mul_f32 v[20:21], v[26:27], v[20:21] op_sel:[1,0] op_sel_hi:[0,0]
	v_pk_fma_f32 v[16:17], v[24:25], v[8:9], v[2:3] op_sel:[0,1,0] op_sel_hi:[1,0,0] neg_lo:[0,0,1] neg_hi:[0,0,1]
	v_mul_f32_e32 v2, v25, v9
	v_pk_mul_f32 v[30:31], v[26:27], v[12:13] op_sel_hi:[1,0]
	v_pk_fma_f32 v[26:27], v[26:27], v[12:13], v[20:21] op_sel_hi:[1,0,1]
	v_pk_fma_f32 v[8:9], v[24:25], v[8:9], v[2:3] op_sel_hi:[1,1,0]
	v_sub_f32_e32 v12, v30, v20
	v_mov_b32_e32 v20, v27
	v_mov_b32_e32 v14, v18
	v_mov_b32_e32 v18, v15
	v_mov_b32_e32 v2, v28
	v_mov_b32_e32 v10, v23
	v_mov_b32_e32 v17, v8
; DEVI void phase_l2(const Params& p, int l, char* smem) {
;     ...
; #pragma unroll
;         for (int q = 0; q < 4; ++q) {
;             float f[8]; unpack8(*(const bf16x8*)(P + (size_t)row * INC + C_KR + half * 32 + q * 8), f);
;             if (lat) {
; #pragma unroll
;                 for (int e = 0; e < 4; ++e) { const int pi = half * 16 + q * 4 + e; const int pos = (pi < 16) ? (t >> 6) : (t & 63);
;                     const f32x2 cs = *(const f32x2*)(rax + (pos * 16 + (pi & 15)) * 2);
;                     const float x1 = f[2 * e], x2 = f[2 * e + 1]; f[2 * e] = x1 * cs[0] - x2 * cs[1]; f[2 * e + 1] = x1 * cs[1] + x2 * cs[0]; }
;             }
;             *(bf16x8*)(dst + q * 8) = pack8(f);
;         }
.LBB0_485:
	s_or_b64 exec, exec, s[16:17]
	v_cvt_pk_bf16_f32 v21, v14, v18
	v_cvt_pk_bf16_f32 v23, v16, v17
	s_nop 1
	v_mov_b64_e32 v[14:15], v[56:57]
	v_mov_b64_e32 v[16:17], v[58:59]
	s_mov_b64 s[14:15], 0x40fae100
	v_lshl_add_u64 v[6:7], v[6:7], 0, s[14:15]
	v_cvt_pk_bf16_f32 v20, v12, v20
	v_cvt_pk_bf16_f32 v22, v2, v10
	global_store_dwordx4 v[6:7], v[20:23], off offset:16
	v_lshlrev_b32_e32 v9, 16, v17
	v_and_b32_e32 v8, 0xffff0000, v17
	v_lshlrev_b32_e32 v12, 16, v14
	v_and_b32_e32 v20, 0xffff0000, v14
	v_lshlrev_b32_e32 v14, 16, v15
	v_and_b32_e32 v18, 0xffff0000, v15
	v_lshlrev_b32_e32 v2, 16, v16
	v_and_b32_e32 v10, 0xffff0000, v16
	v_pk_mov_b32 v[16:17], v[8:9], v[8:9] op_sel:[1,0]
	s_and_saveexec_b64 s[16:17], vcc
	s_cbranch_execz .LBB0_487
	v_cmp_eq_u32_e64 s[38:39], 0, v1
	s_nop 1
	v_cndmask_b32_e64 v15, v13, v11, s[38:39]
	v_lshlrev_b32_e32 v15, 7, v15
	s_nop 1
	v_mov_b64_e32 v[22:23], v[160:161]
	v_mov_b64_e32 v[24:25], v[162:163]
	s_nop 1
	v_mov_b64_e32 v[26:27], v[164:165]
	v_mov_b64_e32 v[28:29], v[166:167]
	v_pk_mul_f32 v[16:17], v[28:29], v[18:19] op_sel:[1,0] op_sel_hi:[0,0]
	v_pk_fma_f32 v[18:19], v[28:29], v[14:15], v[16:17] op_sel_hi:[1,0,1] neg_lo:[0,0,1] neg_hi:[0,0,1]
	v_pk_fma_f32 v[14:15], v[28:29], v[14:15], v[16:17] op_sel_hi:[1,0,1]
	v_pk_mul_f32 v[16:17], v[22:23], v[10:11] op_sel:[1,0] op_sel_hi:[0,0]
	v_pk_fma_f32 v[28:29], v[22:23], v[2:3], v[16:17] op_sel_hi:[1,0,1] neg_lo:[0,0,1] neg_hi:[0,0,1]
	v_pk_fma_f32 v[22:23], v[22:23], v[2:3], v[16:17] op_sel_hi:[1,0,1]
	v_mul_f32_e32 v2, v25, v8
	v_pk_mul_f32 v[20:21], v[26:27], v[20:21] op_sel:[1,0] op_sel_hi:[0,0]
	v_pk_fma_f32 v[16:17], v[24:25], v[8:9], v[2:3] op_sel:[0,1,0] op_sel_hi:[1,0,0] neg_lo:[0,0,1] neg_hi:[0,0,1]
	v_mul_f32_e32 v2, v25, v9
	v_pk_mul_f32 v[30:31], v[26:27], v[12:13] op_sel_hi:[1,0]
	v_pk_fma_f32 v[26:27], v[26:27], v[12:13], v[20:21] op_sel_hi:[1,0,1]
	v_pk_fma_f32 v[8:9], v[24:25], v[8:9], v[2:3] op_sel_hi:[1,1,0]
	v_sub_f32_e32 v12, v30, v20
	v_mov_b32_e32 v20, v27
	v_mov_b32_e32 v14, v18
	v_mov_b32_e32 v18, v15
	v_mov_b32_e32 v2, v28
	v_mov_b32_e32 v10, v23
	v_mov_b32_e32 v17, v8
.LBB0_487:
	s_or_b64 exec, exec, s[16:17]
	v_cvt_pk_bf16_f32 v20, v12, v20
	v_cvt_pk_bf16_f32 v21, v14, v18
	v_cvt_pk_bf16_f32 v22, v2, v10
	v_cvt_pk_bf16_f32 v23, v16, v17
	global_store_dwordx4 v[6:7], v[20:23], off offset:32
	s_nop 1
	v_mov_b64_e32 v[18:19], v[60:61]
	v_mov_b64_e32 v[20:21], v[62:63]
	v_lshlrev_b32_e32 v5, 16, v21
	v_and_b32_e32 v4, 0xffff0000, v21
	v_lshlrev_b32_e32 v10, 16, v18
	v_and_b32_e32 v18, 0xffff0000, v18
	v_lshlrev_b32_e32 v12, 16, v19
	v_and_b32_e32 v16, 0xffff0000, v19
	v_lshlrev_b32_e32 v2, 16, v20
	v_and_b32_e32 v8, 0xffff0000, v20
	v_pk_mov_b32 v[14:15], v[4:5], v[4:5] op_sel:[1,0]
	s_and_saveexec_b64 s[16:17], vcc
	s_cbranch_execz .LBB0_476
	v_cmp_eq_u32_e32 vcc, 0, v1
	s_nop 1
	v_cndmask_b32_e32 v1, v13, v11, vcc
	v_lshlrev_b32_e32 v1, 7, v1
	s_nop 1
	v_mov_b64_e32 v[20:21], v[168:169]
	v_mov_b64_e32 v[22:23], v[170:171]
	s_nop 1
	v_mov_b64_e32 v[24:25], v[172:173]
	v_mov_b64_e32 v[26:27], v[174:175]
	v_pk_mul_f32 v[8:9], v[20:21], v[8:9] op_sel:[1,0] op_sel_hi:[0,0]
	v_pk_mul_f32 v[18:19], v[24:25], v[18:19] op_sel:[1,0] op_sel_hi:[0,0]
	v_pk_mul_f32 v[28:29], v[24:25], v[10:11] op_sel_hi:[1,0]
	v_pk_fma_f32 v[10:11], v[24:25], v[10:11], v[18:19] op_sel_hi:[1,0,1]
	v_pk_mul_f32 v[14:15], v[26:27], v[16:17] op_sel:[1,0] op_sel_hi:[0,0]
	v_pk_fma_f32 v[24:25], v[20:21], v[2:3], v[8:9] op_sel_hi:[1,0,1] neg_lo:[0,0,1] neg_hi:[0,0,1]
	v_pk_fma_f32 v[8:9], v[20:21], v[2:3], v[8:9] op_sel_hi:[1,0,1]
	v_mul_f32_e32 v2, v23, v4
	v_pk_fma_f32 v[16:17], v[26:27], v[12:13], v[14:15] op_sel_hi:[1,0,1] neg_lo:[0,0,1] neg_hi:[0,0,1]
	v_pk_fma_f32 v[12:13], v[26:27], v[12:13], v[14:15] op_sel_hi:[1,0,1]
	v_pk_fma_f32 v[14:15], v[22:23], v[4:5], v[2:3] op_sel:[0,1,0] op_sel_hi:[1,0,0] neg_lo:[0,0,1] neg_hi:[0,0,1]
	v_mul_f32_e32 v2, v23, v5
	v_pk_fma_f32 v[4:5], v[22:23], v[4:5], v[2:3] op_sel_hi:[1,1,0]
	v_sub_f32_e32 v10, v28, v18
	v_mov_b32_e32 v18, v11
	v_mov_b32_e32 v12, v16
	v_mov_b32_e32 v16, v13
	v_mov_b32_e32 v2, v24
	v_mov_b32_e32 v8, v9
	v_mov_b32_e32 v15, v4
	s_branch .LBB0_476
